# xmov
# baseline (speedup 1.0000x reference)
.LBB1_4:
	s_or_b64 exec, exec, s[10:11]
	v_lshl_or_b32 v221, s2, 4, v1
	v_lshlrev_b32_e32 v10, 7, v221
	v_and_or_b32 v0, v0, 31, v10
	v_lshrrev_b32_e32 v3, 5, v220
	v_mul_lo_u32 v160, v0, 27
	v_mov_b32_e32 v161, 0
	s_add_u32 s0, s6, 0x16000
	v_mul_u32_u24_e32 v3, 14, v3
	v_lshl_add_u64 v[0:1], v[160:161], 2, s[4:5]
	v_add_u32_e32 v160, 0x360, v160
	s_addc_u32 s1, s7, 0
	v_lshlrev_b32_e32 v4, 2, v3
	v_mov_b32_e32 v5, v161
	v_lshl_add_u64 v[8:9], v[160:161], 2, s[4:5]
	v_lshl_or_b32 v160, v220, 1, v10
	v_lshl_add_u64 v[6:7], v[0:1], 0, v[4:5]
	v_lshl_add_u64 v[10:11], v[160:161], 2, s[0:1]
	v_or_b32_e32 v160, 0x400, v160
	global_load_dwordx4 v[182:185], v[6:7], off
	global_load_dwordx4 v[178:181], v[6:7], off offset:32
	global_load_dwordx4 v[198:201], v[6:7], off offset:16
	v_lshl_add_u64 v[12:13], v[160:161], 2, s[0:1]
	global_load_dwordx2 v[14:15], v[10:11], off
	global_load_dwordx2 v[16:17], v[12:13], off
	global_load_dword v222, v[0:1], off offset:52
	v_lshl_add_u64 v[0:1], v[8:9], 0, v[4:5]
	global_load_dword v223, v[0:1], off offset:48
	global_load_dwordx4 v[186:189], v[0:1], off offset:32
	global_load_dwordx4 v[194:197], v[0:1], off offset:16
	global_load_dword v225, v[6:7], off offset:48
	global_load_dwordx4 v[190:193], v[0:1], off
	global_load_dword v224, v[8:9], off offset:52
	s_add_u32 s6, s6, 0x216000
	s_load_dwordx2 s[10:11], s[12:13], 0x0
	s_load_dword s18, s[12:13], 0x8
	s_addc_u32 s7, s7, 0
	s_add_i32 s12, 0, 0x16000
	v_add_u32_e32 v228, s12, v2
	v_lshl_add_u32 v1, v220, 3, v228
	v_mov_b32_e32 v160, v161
	s_mov_b32 s16, 0
	v_cmp_gt_u32_e64 s[0:1], 32, v220
	v_cmp_eq_u32_e64 s[2:3], 0, v220
	v_mov_b32_e32 v226, 0x7f
	v_mov_b32_e32 v227, 27
	v_mov_b32_e32 v230, 0
	v_mov_b64_e32 v[218:219], v[160:161]
	s_waitcnt vmcnt(0)
	ds_write2st64_b64 v1, v[14:15], v[16:17] offset1:1
	s_waitcnt vmcnt(0)
	v_mbcnt_lo_u32_b32 v1, -1, 0
	v_mov_b32_e32 v163, v200
	v_mov_b32_e32 v200, v179
	v_mov_b32_e32 v179, v180
	v_mbcnt_hi_u32_b32 v229, -1, v1
	s_waitcnt lgkmcnt(0)
	s_barrier
	s_branch .LBB1_7

.LBB1_6:
	s_waitcnt vmcnt(9)
	s_waitcnt vmcnt(7)
	v_mov_b32_e32 v163, v200
	s_waitcnt vmcnt(5)
	v_mov_b32_e32 v200, v179
	s_cmp_eq_u32 s16, 4
	v_mov_b32_e32 v179, v180
	s_cbranch_scc1 .LBB1_26

.LBB1_12:
	s_and_b32 s12, s19, 1
	s_lshr_b32 s13, s19, 1
	s_add_i32 s16, s19, 1
	v_lshl_add_u32 v231, s13, 3, v221
	s_cmp_lg_u32 s19, 3
	s_cselect_b32 s17, s16, 3
	s_waitcnt lgkmcnt(2)
	v_lshlrev_b32_e32 v2, 7, v231
	s_lshl_b32 s14, s12, 6
	v_or3_b32 v160, v2, s14, v220
	s_waitcnt lgkmcnt(0)
	v_mov_b32_e32 v1, v220
	v_lshl_add_u64 v[2:3], v[160:161], 2, s[6:7]
	global_load_dword v232, v[2:3], off
	s_lshl_b32 s14, s17, 2
	s_and_b32 s14, s14, 24
	s_lshl_b32 s13, s13, 9
	v_lshrrev_b32_e32 v3, 5, v1
	s_cmp_eq_u32 s12, 0
	v_add_u32_e32 v2, s14, v221
	v_lshlrev_b32_e32 v206, 4, v3
	s_cselect_b64 s[14:15], -1, 0
	s_cmp_eq_u32 s12, 1
	v_add3_u32 v149, v228, s13, v206
	s_cselect_b64 s[12:13], -1, 0
	s_lshl_b32 s17, s17, 6
	s_and_b32 s17, s17, 64
	v_lshl_or_b32 v2, v2, 7, s17
	v_lshl_add_u32 v234, v1, 4, 0
	v_and_or_b32 v1, v1, 31, v2
	v_mul_lo_u32 v2, v1, 27
	v_add_u32_e32 v233, 0xc000, v234
	v_mad_u64_u32 v[204:205], s[20:21], v3, 14, v[2:3]
	v_add_u32_e32 v202, 13, v2
	s_waitcnt vmcnt(3)
	v_mul_f32_e32 v1, 0.15915494, v222
	v_cos_f32_e32 v2, v1
	v_sin_f32_e32 v1, v1
	v_add_f32_e32 v2, v2, v2
	v_cndmask_b32_e64 v3, v2, v1, s[0:1]
	v_mul_f32_e32 v1, v1, v2
	v_fma_f32 v2, v2, v2, -2.0
	v_cndmask_b32_e64 v4, v2, v1, s[0:1]
	v_mul_f32_e32 v207, v1, v2
	v_fma_f32 v208, v2, v2, -2.0
	v_mul_f32_e32 v2, 0.15915494, v182
	v_cvt_pk_fp8_f32 v131, v225, v3
	v_cos_f32_e32 v3, v2
	v_sin_f32_e32 v2, v2
	v_cndmask_b32_e64 v1, v208, v207, s[0:1]
	v_cvt_pk_fp8_f32 v131, v4, v1 op_sel:[0,0,1]
	v_add_f32_e32 v1, v3, v3
	v_cvt_pk_f16_f32 v1, v2, v1
	v_cvt_pk_fp8_f32 v128, v182, v183
	v_cvt_scalef32_pk_fp8_f16 v132, v1, 1.0
	v_pk_fma_f16 v1, v1, v1, -2.0 op_sel:[1,0,1] op_sel_hi:[1,1,0]
	v_mul_f32_e32 v0, 0.15915494, v183
	v_cvt_scalef32_pk_fp8_f16 v132, v1, 1.0 op_sel:[0,0,1]
	v_pk_fma_f16 v1, v1, v1, -2.0 op_sel:[0,1,1] op_sel_hi:[1,1,0]
	v_cos_f32_e32 v2, v0
	v_cvt_scalef32_pk_fp8_f16 v133, v1, 1.0
	v_pk_fma_f16 v1, v1, v1, -2.0 op_sel:[0,1,1] op_sel_hi:[1,1,0]
	v_sin_f32_e32 v0, v0
	v_cvt_scalef32_pk_fp8_f16 v133, v1, 1.0 op_sel:[0,0,1]
	v_pk_fma_f16 v1, v1, v1, -2.0 op_sel:[0,1,1] op_sel_hi:[1,1,0]
	s_nop 0
	v_cvt_scalef32_pk_fp8_f16 v134, v1, 1.0
	v_pk_fma_f16 v1, v1, v1, -2.0 op_sel:[0,1,1] op_sel_hi:[1,1,0]
	s_nop 0
	v_cvt_scalef32_pk_fp8_f16 v134, v1, 1.0 op_sel:[0,0,1]
	v_add_f32_e32 v1, v2, v2
	v_cvt_pk_f16_f32 v0, v0, v1
	v_cvt_scalef32_pk_fp8_f16 v135, v0, 1.0
	v_pk_fma_f16 v24, v0, v0, -2.0 op_sel:[1,0,1] op_sel_hi:[1,1,0]
	s_waitcnt vmcnt(2)
	v_mul_f32_e32 v0, 0.15915494, v224
	v_cos_f32_e32 v1, v0
	v_sin_f32_e32 v0, v0
	v_add_f32_e32 v1, v1, v1
	v_cndmask_b32_e64 v2, v1, v0, s[0:1]
	v_mul_f32_e32 v0, v0, v1
	v_fma_f32 v1, v1, v1, -2.0
	v_cndmask_b32_e64 v3, v1, v0, s[0:1]
	v_mul_f32_e32 v209, v0, v1
	v_fma_f32 v210, v1, v1, -2.0
	v_mul_f32_e32 v1, 0.15915494, v190
	s_waitcnt vmcnt(1)
	v_cvt_pk_fp8_f32 v19, v223, v2
	v_cos_f32_e32 v2, v1
	v_sin_f32_e32 v1, v1
	v_cndmask_b32_e64 v0, v210, v209, s[0:1]
	v_cvt_pk_fp8_f32 v19, v3, v0 op_sel:[0,0,1]
	v_add_f32_e32 v0, v2, v2
	v_cvt_pk_f16_f32 v0, v1, v0
	v_cvt_scalef32_pk_fp8_f16 v20, v0, 1.0
	v_pk_fma_f16 v0, v0, v0, -2.0 op_sel:[1,0,1] op_sel_hi:[1,1,0]
	v_mul_f32_e32 v1, 0.15915494, v191
	v_cvt_scalef32_pk_fp8_f16 v135, v24, 1.0 op_sel:[0,0,1]
	v_cvt_scalef32_pk_fp8_f16 v20, v0, 1.0 op_sel:[0,0,1]
	v_pk_fma_f16 v0, v0, v0, -2.0 op_sel:[0,1,1] op_sel_hi:[1,1,0]
	v_cos_f32_e32 v2, v1
	v_pk_fma_f16 v24, v24, v24, -2.0 op_sel:[0,1,1] op_sel_hi:[1,1,0]
	v_cvt_scalef32_pk_fp8_f16 v21, v0, 1.0
	v_pk_fma_f16 v0, v0, v0, -2.0 op_sel:[0,1,1] op_sel_hi:[1,1,0]
	v_sin_f32_e32 v1, v1
	v_pk_fma_f16 v35, v24, v24, -2.0 op_sel:[0,1,1] op_sel_hi:[1,1,0]
	v_cvt_pk_fp8_f32 v128, v184, v185 op_sel:[0,0,1]
	v_cvt_scalef32_pk_fp8_f16 v21, v0, 1.0 op_sel:[0,0,1]
	v_pk_fma_f16 v0, v0, v0, -2.0 op_sel:[0,1,1] op_sel_hi:[1,1,0]
	v_pk_fma_f16 v36, v35, v35, -2.0 op_sel:[0,1,1] op_sel_hi:[1,1,0]
	v_mul_f32_e32 v25, 0.15915494, v184
	v_cvt_pk_fp8_f32 v129, v198, v199
	v_cvt_pk_fp8_f32 v130, v178, v200
	v_cvt_pk_fp8_f32 v16, v190, v191
	v_cvt_pk_fp8_f32 v17, v194, v195
	v_cvt_pk_fp8_f32 v18, v186, v187
	v_cvt_scalef32_pk_fp8_f16 v22, v0, 1.0
	v_pk_fma_f16 v0, v0, v0, -2.0 op_sel:[0,1,1] op_sel_hi:[1,1,0]
	v_pk_fma_f16 v37, v36, v36, -2.0 op_sel:[0,1,1] op_sel_hi:[1,1,0]
	v_cvt_scalef32_pk_fp8_f16 v137, v36, 1.0
	v_cos_f32_e32 v36, v25
	v_cvt_scalef32_pk_fp8_f16 v22, v0, 1.0 op_sel:[0,0,1]
	v_add_f32_e32 v0, v2, v2
	v_sin_f32_e32 v25, v25
	v_cvt_pk_f16_f32 v0, v1, v0
	v_mov_b32_e32 v160, v204
	v_cvt_scalef32_pk_fp8_f16 v23, v0, 1.0
	v_pk_fma_f16 v34, v0, v0, -2.0 op_sel:[1,0,1] op_sel_hi:[1,1,0]
	ds_read_b128 v[26:29], v234
	ds_read_b128 v[30:33], v234 offset:1024
	ds_read_b128 v[8:11], v234 offset:2048
	ds_read_b128 v[12:15], v234 offset:3072
	ds_read_b128 v[0:3], v234 offset:4096
	ds_read_b128 v[4:7], v234 offset:5120
	ds_read_b128 v[152:155], v234 offset:6144
	ds_read_b128 v[156:159], v234 offset:7168
	ds_read_b128 v[96:99], v149
	ds_read_b128 v[100:103], v149 offset:32
	ds_read_b128 v[104:107], v149 offset:64
	ds_read_b128 v[108:111], v149 offset:96
	v_cvt_pk_fp8_f32 v129, v163, v201 op_sel:[0,0,1]
	v_cvt_pk_fp8_f32 v130, v179, v181 op_sel:[0,0,1]
	v_cvt_pk_fp8_f32 v16, v192, v193 op_sel:[0,0,1]
	v_cvt_pk_fp8_f32 v17, v196, v197 op_sel:[0,0,1]
	v_cvt_pk_fp8_f32 v18, v188, v189 op_sel:[0,0,1]
	v_cvt_scalef32_pk_fp8_f16 v136, v24, 1.0
	v_add_f32_e32 v24, v36, v36
	v_cvt_pk_f16_f32 v24, v25, v24
	v_pk_fma_f16 v25, v24, v24, -2.0 op_sel:[1,0,1] op_sel_hi:[1,1,0]
	v_cvt_scalef32_pk_fp8_f16 v138, v24, 1.0
	v_cvt_scalef32_pk_fp8_f16 v23, v34, 1.0 op_sel:[0,0,1]
	v_cvt_scalef32_pk_fp8_f16 v136, v35, 1.0 op_sel:[0,0,1]
	v_pk_fma_f16 v35, v25, v25, -2.0 op_sel:[0,1,1] op_sel_hi:[1,1,0]
	v_cvt_scalef32_pk_fp8_f16 v138, v25, 1.0 op_sel:[0,0,1]
	v_mul_f32_e32 v25, 0.15915494, v185
	s_waitcnt lgkmcnt(0)
	v_mfma_scale_f32_32x32x64_f8f6f4 v[112:127], v[26:33], v[16:23], v[96:111], v227, v226 op_sel_hi:[0,0,0]
	v_cvt_scalef32_pk_fp8_f16 v139, v35, 1.0
	v_pk_fma_f16 v35, v35, v35, -2.0 op_sel:[0,1,1] op_sel_hi:[1,1,0]
	s_nop 0
	v_pk_fma_f16 v24, v35, v35, -2.0 op_sel:[0,1,1] op_sel_hi:[1,1,0]
	ds_read_b128 v[64:67], v149 offset:128
	ds_read_b128 v[68:71], v149 offset:160
	ds_read_b128 v[72:75], v149 offset:192
	ds_read_b128 v[76:79], v149 offset:224
	v_cvt_scalef32_pk_fp8_f16 v140, v24, 1.0
	v_pk_fma_f16 v24, v24, v24, -2.0 op_sel:[0,1,1] op_sel_hi:[1,1,0]
	v_cvt_scalef32_pk_fp8_f16 v137, v37, 1.0 op_sel:[0,0,1]
	v_cvt_scalef32_pk_fp8_f16 v140, v24, 1.0 op_sel:[0,0,1]
	v_cvt_scalef32_pk_fp8_f16 v139, v35, 1.0 op_sel:[0,0,1]
	v_mfma_scale_f32_32x32x64_f8f6f4 v[96:111], v[26:33], v[128:135], v[96:111], v227, v226 op_sel_hi:[0,0,0]
	v_cos_f32_e32 v26, v25
	v_sin_f32_e32 v25, v25
	v_mul_f32_e32 v30, 0.15915494, v192
	v_mul_f32_e32 v31, 0.15915494, v193
	v_add_f32_e32 v24, v26, v26
	v_cvt_pk_f16_f32 v24, v25, v24
	v_cvt_scalef32_pk_fp8_f16 v141, v24, 1.0
	v_pk_fma_f16 v24, v24, v24, -2.0 op_sel:[1,0,1] op_sel_hi:[1,1,0]
	s_nop 0
	v_cvt_scalef32_pk_fp8_f16 v141, v24, 1.0 op_sel:[0,0,1]
	v_pk_fma_f16 v26, v24, v24, -2.0 op_sel:[0,1,1] op_sel_hi:[1,1,0]
	v_lshl_add_u64 v[24:25], v[160:161], 2, s[4:5]
	v_pk_fma_f16 v27, v26, v26, -2.0 op_sel:[0,1,1] op_sel_hi:[1,1,0]
	s_nop 0
	v_pk_fma_f16 v28, v27, v27, -2.0 op_sel:[0,1,1] op_sel_hi:[1,1,0]
	s_waitcnt lgkmcnt(0)
	v_mfma_scale_f32_32x32x64_f8f6f4 v[80:95], v[8:15], v[16:23], v[64:79], v227, v226 op_sel_hi:[0,0,0]
	global_load_dwordx4 v[182:185], v[24:25], off
	global_load_dwordx4 v[190:193], v[24:25], off offset:3456
	v_cos_f32_e32 v25, v31
	v_pk_fma_f16 v29, v28, v28, -2.0 op_sel:[0,1,1] op_sel_hi:[1,1,0]
	v_cvt_scalef32_pk_fp8_f16 v143, v28, 1.0
	v_cvt_scalef32_pk_fp8_f16 v142, v26, 1.0
	v_cvt_scalef32_pk_fp8_f16 v143, v29, 1.0 op_sel:[0,0,1]
	v_cvt_scalef32_pk_fp8_f16 v142, v27, 1.0 op_sel:[0,0,1]
	v_add_f32_e32 v150, v25, v25
	v_mfma_scale_f32_32x32x64_f8f6f4 v[64:79], v[8:15], v[128:135], v[64:79], v227, v226 op_sel_hi:[0,0,0]
	v_pk_fma_f16 v8, v34, v34, -2.0 op_sel:[0,1,1] op_sel_hi:[1,1,0]
	ds_read_b128 v[32:35], v149 offset:256
	ds_read_b128 v[36:39], v149 offset:288
	ds_read_b128 v[40:43], v149 offset:320
	ds_read_b128 v[44:47], v149 offset:352
	v_pk_fma_f16 v9, v8, v8, -2.0 op_sel:[0,1,1] op_sel_hi:[1,1,0]
	v_cvt_scalef32_pk_fp8_f16 v144, v8, 1.0
	v_pk_fma_f16 v10, v9, v9, -2.0 op_sel:[0,1,1] op_sel_hi:[1,1,0]
	v_cvt_scalef32_pk_fp8_f16 v144, v9, 1.0 op_sel:[0,0,1]
	v_pk_fma_f16 v11, v10, v10, -2.0 op_sel:[0,1,1] op_sel_hi:[1,1,0]
	v_cvt_scalef32_pk_fp8_f16 v145, v10, 1.0
	v_cos_f32_e32 v10, v30
	v_cvt_scalef32_pk_fp8_f16 v145, v11, 1.0 op_sel:[0,0,1]
	v_sin_f32_e32 v11, v30
	v_add_f32_e32 v8, v10, v10
	v_cvt_pk_f16_f32 v8, v11, v8
	v_pk_fma_f16 v9, v8, v8, -2.0 op_sel:[1,0,1] op_sel_hi:[1,1,0]
	v_cvt_scalef32_pk_fp8_f16 v146, v8, 1.0
	v_pk_fma_f16 v10, v9, v9, -2.0 op_sel:[0,1,1] op_sel_hi:[1,1,0]
	s_waitcnt lgkmcnt(0)
	v_mfma_scale_f32_32x32x64_f8f6f4 v[48:63], v[0:7], v[16:23], v[32:47], v227, v226 op_sel_hi:[0,0,0]
	v_cvt_scalef32_pk_fp8_f16 v147, v10, 1.0
	v_pk_fma_f16 v10, v10, v10, -2.0 op_sel:[0,1,1] op_sel_hi:[1,1,0]
	v_cvt_scalef32_pk_fp8_f16 v146, v9, 1.0 op_sel:[0,0,1]
	v_cvt_scalef32_pk_fp8_f16 v147, v10, 1.0 op_sel:[0,0,1]
	v_pk_fma_f16 v24, v10, v10, -2.0 op_sel:[0,1,1] op_sel_hi:[1,1,0]
	s_nop 0
	v_cvt_scalef32_pk_fp8_f16 v148, v24, 1.0
	v_pk_fma_f16 v24, v24, v24, -2.0 op_sel:[0,1,1] op_sel_hi:[1,1,0]
	s_nop 0
	v_cvt_scalef32_pk_fp8_f16 v148, v24, 1.0 op_sel:[0,0,1]
	v_mfma_scale_f32_32x32x64_f8f6f4 v[32:47], v[0:7], v[128:135], v[32:47], v227, v226 op_sel_hi:[0,0,0]
	ds_read_b128 v[0:3], v149 offset:384
	ds_read_b128 v[4:7], v149 offset:416
	ds_read_b128 v[8:11], v149 offset:448
	ds_read_b128 v[12:15], v149 offset:480
	v_sin_f32_e32 v149, v31
	s_nop 0
	v_cvt_pk_f16_f32 v150, v149, v150
	v_cvt_scalef32_pk_fp8_f16 v149, v150, 1.0
	v_pk_fma_f16 v150, v150, v150, -2.0 op_sel:[1,0,1] op_sel_hi:[1,1,0]
	s_nop 0
	v_pk_fma_f16 v160, v150, v150, -2.0 op_sel:[0,1,1] op_sel_hi:[1,1,0]
	v_cvt_scalef32_pk_fp8_f16 v149, v150, 1.0 op_sel:[0,0,1]
	v_pk_fma_f16 v164, v160, v160, -2.0 op_sel:[0,1,1] op_sel_hi:[1,1,0]
	s_nop 0
	v_pk_fma_f16 v150, v164, v164, -2.0 op_sel:[0,1,1] op_sel_hi:[1,1,0]
	s_waitcnt lgkmcnt(0)
	v_mfma_scale_f32_32x32x64_f8f6f4 v[16:31], v[152:159], v[16:23], v[0:15], v227, v226 op_sel_hi:[0,0,0]
	v_pk_fma_f16 v165, v150, v150, -2.0 op_sel:[0,1,1] op_sel_hi:[1,1,0]
	v_cvt_scalef32_pk_fp8_f16 v151, v150, 1.0
	v_cvt_scalef32_pk_fp8_f16 v150, v160, 1.0
	v_cvt_scalef32_pk_fp8_f16 v151, v165, 1.0 op_sel:[0,0,1]
	v_cvt_scalef32_pk_fp8_f16 v150, v164, 1.0 op_sel:[0,0,1]
	v_mfma_scale_f32_32x32x64_f8f6f4 v[0:15], v[152:159], v[128:135], v[0:15], v227, v226 op_sel_hi:[0,0,0]
	v_mul_f32_e32 v128, 0.15915494, v198
	v_cos_f32_e32 v129, v128
	v_sin_f32_e32 v128, v128
	v_mul_f32_e32 v133, 0.15915494, v199
	v_cos_f32_e32 v134, v133
	v_add_f32_e32 v129, v129, v129
	v_cvt_pk_f16_f32 v130, v128, v129
	v_pk_fma_f16 v131, v130, v130, -2.0 op_sel:[1,0,1] op_sel_hi:[1,1,0]
	v_sin_f32_e32 v133, v133
	v_pk_fma_f16 v128, v131, v131, -2.0 op_sel:[0,1,1] op_sel_hi:[1,1,0]
	s_nop 0
	v_pk_fma_f16 v132, v128, v128, -2.0 op_sel:[0,1,1] op_sel_hi:[1,1,0]
	v_cvt_scalef32_pk_fp8_f16 v129, v128, 1.0
	v_cvt_scalef32_pk_fp8_f16 v128, v130, 1.0
	v_add_f32_e32 v130, v134, v134
	v_cvt_scalef32_pk_fp8_f16 v128, v131, 1.0 op_sel:[0,0,1]
	v_cvt_pk_f16_f32 v130, v133, v130
	v_cvt_scalef32_pk_fp8_f16 v129, v132, 1.0 op_sel:[0,0,1]
	v_cvt_scalef32_pk_fp8_f16 v131, v130, 1.0
	v_pk_fma_f16 v133, v130, v130, -2.0 op_sel:[1,0,1] op_sel_hi:[1,1,0]
	v_pk_fma_f16 v132, v132, v132, -2.0 op_sel:[0,1,1] op_sel_hi:[1,1,0]
	ds_read_b128 v[152:155], v234 offset:8192
	ds_read_b128 v[156:159], v234 offset:9216
	ds_read_b128 v[164:167], v234 offset:10240
	ds_read_b128 v[168:171], v234 offset:11264
	ds_read_b128 v[236:239], v234 offset:12288
	ds_read_b128 v[240:243], v234 offset:13312
	v_cvt_scalef32_pk_fp8_f16 v130, v132, 1.0
	v_pk_fma_f16 v132, v132, v132, -2.0 op_sel:[0,1,1] op_sel_hi:[1,1,0]
	v_mul_f32_e32 v135, 0.15915494, v163
	s_waitcnt lgkmcnt(4)
	v_mfma_scale_f32_32x32x64_f8f6f4 v[96:111], v[152:159], v[136:143], v[96:111], v227, v226 op_sel_hi:[0,0,0]
	v_cvt_scalef32_pk_fp8_f16 v131, v133, 1.0 op_sel:[0,0,1]
	v_pk_fma_f16 v133, v133, v133, -2.0 op_sel:[0,1,1] op_sel_hi:[1,1,0]
	v_cvt_scalef32_pk_fp8_f16 v130, v132, 1.0 op_sel:[0,0,1]
	v_cvt_scalef32_pk_fp8_f16 v132, v133, 1.0
	v_pk_fma_f16 v133, v133, v133, -2.0 op_sel:[0,1,1] op_sel_hi:[1,1,0]
	ds_read_b128 v[244:247], v234 offset:14336
	ds_read_b128 v[248:251], v234 offset:15360
	v_pk_fma_f16 v134, v133, v133, -2.0 op_sel:[0,1,1] op_sel_hi:[1,1,0]
	v_cvt_scalef32_pk_fp8_f16 v132, v133, 1.0 op_sel:[0,0,1]
	v_cvt_scalef32_pk_fp8_f16 v133, v134, 1.0
	v_pk_fma_f16 v134, v134, v134, -2.0 op_sel:[0,1,1] op_sel_hi:[1,1,0]
	s_nop 0
	v_cvt_scalef32_pk_fp8_f16 v133, v134, 1.0 op_sel:[0,0,1]
	v_mfma_scale_f32_32x32x64_f8f6f4 v[112:127], v[152:159], v[144:151], v[112:127], v227, v226 op_sel_hi:[0,0,0]
	v_cos_f32_e32 v152, v135
	v_sin_f32_e32 v135, v135
	v_mul_f32_e32 v154, 0.15915494, v194
	v_cos_f32_e32 v155, v154
	v_add_f32_e32 v134, v152, v152
	v_cvt_pk_f16_f32 v152, v135, v134
	v_pk_fma_f16 v153, v152, v152, -2.0 op_sel:[1,0,1] op_sel_hi:[1,1,0]
	v_sin_f32_e32 v154, v154
	v_pk_fma_f16 v134, v153, v153, -2.0 op_sel:[0,1,1] op_sel_hi:[1,1,0]
	s_nop 0
	v_pk_fma_f16 v160, v134, v134, -2.0 op_sel:[0,1,1] op_sel_hi:[1,1,0]
	v_cvt_scalef32_pk_fp8_f16 v135, v134, 1.0
	v_cvt_scalef32_pk_fp8_f16 v134, v152, 1.0
	v_add_f32_e32 v152, v155, v155
	s_waitcnt lgkmcnt(4)
	v_mfma_scale_f32_32x32x64_f8f6f4 v[64:79], v[164:171], v[136:143], v[64:79], v227, v226 op_sel_hi:[0,0,0]
	v_mul_f32_e32 v157, 0.15915494, v195
	v_cvt_pk_f16_f32 v154, v154, v152
	v_cos_f32_e32 v158, v157
	v_pk_fma_f16 v155, v154, v154, -2.0 op_sel:[1,0,1] op_sel_hi:[1,1,0]
	v_sin_f32_e32 v157, v157
	v_pk_fma_f16 v152, v155, v155, -2.0 op_sel:[0,1,1] op_sel_hi:[1,1,0]
	v_cvt_scalef32_pk_fp8_f16 v134, v153, 1.0 op_sel:[0,0,1]
	v_pk_fma_f16 v156, v152, v152, -2.0 op_sel:[0,1,1] op_sel_hi:[1,1,0]
	v_cvt_scalef32_pk_fp8_f16 v153, v152, 1.0
	v_cvt_scalef32_pk_fp8_f16 v152, v154, 1.0
	v_add_f32_e32 v154, v158, v158
	v_mul_f32_e32 v159, 0.15915494, v196
	v_cvt_scalef32_pk_fp8_f16 v152, v155, 1.0 op_sel:[0,0,1]
	v_mfma_scale_f32_32x32x64_f8f6f4 v[80:95], v[164:171], v[144:151], v[80:95], v227, v226 op_sel_hi:[0,0,0]
	v_cvt_pk_f16_f32 v154, v157, v154
	v_cvt_scalef32_pk_fp8_f16 v153, v156, 1.0 op_sel:[0,0,1]
	v_cvt_scalef32_pk_fp8_f16 v155, v154, 1.0
	v_pk_fma_f16 v156, v156, v156, -2.0 op_sel:[0,1,1] op_sel_hi:[1,1,0]
	v_pk_fma_f16 v157, v154, v154, -2.0 op_sel:[1,0,1] op_sel_hi:[1,1,0]
	v_cvt_scalef32_pk_fp8_f16 v154, v156, 1.0
	v_pk_fma_f16 v156, v156, v156, -2.0 op_sel:[0,1,1] op_sel_hi:[1,1,0]
	v_cvt_scalef32_pk_fp8_f16 v155, v157, 1.0 op_sel:[0,0,1]
	v_pk_fma_f16 v157, v157, v157, -2.0 op_sel:[0,1,1] op_sel_hi:[1,1,0]
	v_cvt_scalef32_pk_fp8_f16 v154, v156, 1.0 op_sel:[0,0,1]
	v_cvt_scalef32_pk_fp8_f16 v156, v157, 1.0
	v_pk_fma_f16 v157, v157, v157, -2.0 op_sel:[0,1,1] op_sel_hi:[1,1,0]
	s_waitcnt lgkmcnt(0)
	v_mfma_scale_f32_32x32x64_f8f6f4 v[0:15], v[244:251], v[136:143], v[0:15], v227, v226 op_sel_hi:[0,0,0]
	v_cvt_scalef32_pk_fp8_f16 v156, v157, 1.0 op_sel:[0,0,1]
	v_pk_fma_f16 v158, v157, v157, -2.0 op_sel:[0,1,1] op_sel_hi:[1,1,0]
	v_cvt_scalef32_pk_fp8_f16 v135, v160, 1.0 op_sel:[0,0,1]
	v_cvt_scalef32_pk_fp8_f16 v157, v158, 1.0
	v_mfma_scale_f32_32x32x64_f8f6f4 v[32:47], v[236:243], v[136:143], v[32:47], v227, v226 op_sel_hi:[0,0,0]
	v_cos_f32_e32 v136, v159
	v_sin_f32_e32 v137, v159
	v_pk_fma_f16 v138, v158, v158, -2.0 op_sel:[0,1,1] op_sel_hi:[1,1,0]
	v_add_f32_e32 v136, v136, v136
	v_cvt_pk_f16_f32 v136, v137, v136
	v_pk_fma_f16 v137, v136, v136, -2.0 op_sel:[1,0,1] op_sel_hi:[1,1,0]
	v_cvt_scalef32_pk_fp8_f16 v157, v138, 1.0 op_sel:[0,0,1]
	v_pk_fma_f16 v138, v137, v137, -2.0 op_sel:[0,1,1] op_sel_hi:[1,1,0]
	s_nop 0
	v_pk_fma_f16 v180, v138, v138, -2.0 op_sel:[0,1,1] op_sel_hi:[1,1,0]
	v_cvt_scalef32_pk_fp8_f16 v159, v138, 1.0
	v_cvt_scalef32_pk_fp8_f16 v158, v136, 1.0
	v_cvt_scalef32_pk_fp8_f16 v159, v180, 1.0 op_sel:[0,0,1]
	v_cvt_scalef32_pk_fp8_f16 v158, v137, 1.0 op_sel:[0,0,1]
	v_mfma_scale_f32_32x32x64_f8f6f4 v[48:63], v[236:243], v[144:151], v[48:63], v227, v226 op_sel_hi:[0,0,0]
	v_mfma_scale_f32_32x32x64_f8f6f4 v[16:31], v[244:251], v[144:151], v[16:31], v227, v226 op_sel_hi:[0,0,0]
	ds_read_b128 v[140:143], v234 offset:16384
	ds_read_b128 v[144:147], v234 offset:17408
	ds_read_b128 v[236:239], v234 offset:18432
	ds_read_b128 v[240:243], v234 offset:19456
	ds_read_b128 v[170:173], v234 offset:20480
	ds_read_b128 v[174:177], v234 offset:21504
	s_waitcnt lgkmcnt(4)
	v_mfma_scale_f32_32x32x64_f8f6f4 v[96:111], v[140:147], v[128:135], v[96:111], v227, v226 op_sel_hi:[0,0,0]
	v_pk_fma_f16 v139, v160, v160, -2.0 op_sel:[0,1,1] op_sel_hi:[1,1,0]
	v_mov_b32_e32 v160, v204
	ds_read_b128 v[162:165], v234 offset:22528
	ds_read_b128 v[166:169], v234 offset:23552
	v_mul_f32_e32 v136, 0.15915494, v201
	v_cos_f32_e32 v137, v136
	v_sin_f32_e32 v136, v136
	v_mul_f32_e32 v150, 0.15915494, v186
	v_cos_f32_e32 v151, v150
	v_add_f32_e32 v137, v137, v137
	v_cvt_pk_f16_f32 v136, v136, v137
	v_pk_fma_f16 v138, v136, v136, -2.0 op_sel:[1,0,1] op_sel_hi:[1,1,0]
	v_cvt_scalef32_pk_fp8_f16 v137, v136, 1.0
	v_mfma_scale_f32_32x32x64_f8f6f4 v[112:127], v[140:147], v[152:159], v[112:127], v227, v226 op_sel_hi:[0,0,0]
	v_mul_f32_e32 v140, 0.15915494, v178
	v_cos_f32_e32 v141, v140
	v_sin_f32_e32 v140, v140
	v_mul_f32_e32 v143, 0.15915494, v200
	v_cos_f32_e32 v144, v143
	v_add_f32_e32 v141, v141, v141
	v_cvt_pk_f16_f32 v141, v140, v141
	v_sin_f32_e32 v143, v143
	v_cvt_scalef32_pk_fp8_f16 v140, v141, 1.0
	v_pk_fma_f16 v141, v141, v141, -2.0 op_sel:[1,0,1] op_sel_hi:[1,1,0]
	v_mul_f32_e32 v146, 0.15915494, v197
	v_pk_fma_f16 v142, v141, v141, -2.0 op_sel:[0,1,1] op_sel_hi:[1,1,0]
	v_cvt_scalef32_pk_fp8_f16 v140, v141, 1.0 op_sel:[0,0,1]
	v_cvt_scalef32_pk_fp8_f16 v141, v142, 1.0
	v_pk_fma_f16 v145, v142, v142, -2.0 op_sel:[0,1,1] op_sel_hi:[1,1,0]
	v_add_f32_e32 v142, v144, v144
	v_cvt_pk_f16_f32 v144, v143, v142
	v_lshl_add_u64 v[142:143], v[160:161], 2, s[4:5]
	global_load_dwordx4 v[198:201], v[142:143], off offset:16
	global_load_dwordx4 v[194:197], v[142:143], off offset:3472
	v_cvt_scalef32_pk_fp8_f16 v141, v145, 1.0 op_sel:[0,0,1]
	v_pk_fma_f16 v160, v144, v144, -2.0 op_sel:[1,0,1] op_sel_hi:[1,1,0]
	v_cvt_scalef32_pk_fp8_f16 v143, v144, 1.0
	v_pk_fma_f16 v144, v145, v145, -2.0 op_sel:[0,1,1] op_sel_hi:[1,1,0]
	v_cos_f32_e32 v145, v146
	v_sin_f32_e32 v146, v146
	v_pk_fma_f16 v148, v138, v138, -2.0 op_sel:[0,1,1] op_sel_hi:[1,1,0]
	v_cvt_scalef32_pk_fp8_f16 v136, v139, 1.0
	v_pk_fma_f16 v139, v139, v139, -2.0 op_sel:[0,1,1] op_sel_hi:[1,1,0]
	v_pk_fma_f16 v149, v148, v148, -2.0 op_sel:[0,1,1] op_sel_hi:[1,1,0]
	v_cvt_scalef32_pk_fp8_f16 v142, v144, 1.0
	v_pk_fma_f16 v144, v144, v144, -2.0 op_sel:[0,1,1] op_sel_hi:[1,1,0]
	v_cvt_scalef32_pk_fp8_f16 v137, v138, 1.0 op_sel:[0,0,1]
	v_cvt_scalef32_pk_fp8_f16 v136, v139, 1.0 op_sel:[0,0,1]
	v_pk_fma_f16 v138, v149, v149, -2.0 op_sel:[0,1,1] op_sel_hi:[1,1,0]
	v_cvt_scalef32_pk_fp8_f16 v142, v144, 1.0 op_sel:[0,0,1]
	v_add_f32_e32 v144, v145, v145
	v_cvt_scalef32_pk_fp8_f16 v139, v138, 1.0
	v_pk_fma_f16 v138, v138, v138, -2.0 op_sel:[0,1,1] op_sel_hi:[1,1,0]
	s_waitcnt lgkmcnt(4)
	v_mfma_scale_f32_32x32x64_f8f6f4 v[64:79], v[236:243], v[128:135], v[64:79], v227, v226 op_sel_hi:[0,0,0]
	v_cvt_pk_f16_f32 v144, v146, v144
	v_cvt_scalef32_pk_fp8_f16 v139, v138, 1.0 op_sel:[0,0,1]
	v_pk_fma_f16 v146, v144, v144, -2.0 op_sel:[1,0,1] op_sel_hi:[1,1,0]
	v_cvt_scalef32_pk_fp8_f16 v138, v148, 1.0
	v_cvt_scalef32_pk_fp8_f16 v145, v144, 1.0
	v_pk_fma_f16 v147, v180, v180, -2.0 op_sel:[0,1,1] op_sel_hi:[1,1,0]
	v_pk_fma_f16 v148, v146, v146, -2.0 op_sel:[0,1,1] op_sel_hi:[1,1,0]
	v_cvt_scalef32_pk_fp8_f16 v138, v149, 1.0 op_sel:[0,0,1]
	v_cvt_scalef32_pk_fp8_f16 v144, v147, 1.0
	v_pk_fma_f16 v147, v147, v147, -2.0 op_sel:[0,1,1] op_sel_hi:[1,1,0]
	v_pk_fma_f16 v149, v148, v148, -2.0 op_sel:[0,1,1] op_sel_hi:[1,1,0]
	v_cvt_scalef32_pk_fp8_f16 v145, v146, 1.0 op_sel:[0,0,1]
	v_mfma_scale_f32_32x32x64_f8f6f4 v[80:95], v[236:243], v[152:159], v[80:95], v227, v226 op_sel_hi:[0,0,0]
	v_pk_fma_f16 v146, v149, v149, -2.0 op_sel:[0,1,1] op_sel_hi:[1,1,0]
	v_cvt_scalef32_pk_fp8_f16 v144, v147, 1.0 op_sel:[0,0,1]
	v_cvt_scalef32_pk_fp8_f16 v147, v146, 1.0
	v_pk_fma_f16 v146, v146, v146, -2.0 op_sel:[0,1,1] op_sel_hi:[1,1,0]
	v_sin_f32_e32 v150, v150
	v_cvt_scalef32_pk_fp8_f16 v147, v146, 1.0 op_sel:[0,0,1]
	v_cvt_scalef32_pk_fp8_f16 v146, v148, 1.0
	v_add_f32_e32 v148, v151, v151
	v_mul_f32_e32 v151, 0.15915494, v187
	v_cvt_scalef32_pk_fp8_f16 v146, v149, 1.0 op_sel:[0,0,1]
	v_cvt_pk_f16_f32 v149, v150, v148
	v_cvt_scalef32_pk_fp8_f16 v148, v149, 1.0
	s_waitcnt lgkmcnt(0)
	v_mfma_scale_f32_32x32x64_f8f6f4 v[0:15], v[162:169], v[128:135], v[0:15], v227, v226 op_sel_hi:[0,0,0]
	v_pk_fma_f16 v149, v149, v149, -2.0 op_sel:[1,0,1] op_sel_hi:[1,1,0]
	v_cvt_scalef32_pk_fp8_f16 v143, v160, 1.0 op_sel:[0,0,1]
	v_pk_fma_f16 v150, v149, v149, -2.0 op_sel:[0,1,1] op_sel_hi:[1,1,0]
	v_cvt_scalef32_pk_fp8_f16 v148, v149, 1.0 op_sel:[0,0,1]
	v_cvt_scalef32_pk_fp8_f16 v149, v150, 1.0
	v_mfma_scale_f32_32x32x64_f8f6f4 v[32:47], v[170:177], v[128:135], v[32:47], v227, v226 op_sel_hi:[0,0,0]
	v_cos_f32_e32 v128, v151
	v_sin_f32_e32 v129, v151
	v_pk_fma_f16 v130, v150, v150, -2.0 op_sel:[0,1,1] op_sel_hi:[1,1,0]
	v_add_f32_e32 v128, v128, v128
	v_cvt_pk_f16_f32 v128, v129, v128
	v_pk_fma_f16 v203, v128, v128, -2.0 op_sel:[1,0,1] op_sel_hi:[1,1,0]
	v_cvt_scalef32_pk_fp8_f16 v151, v128, 1.0
	v_pk_fma_f16 v128, v130, v130, -2.0 op_sel:[0,1,1] op_sel_hi:[1,1,0]
	s_nop 0
	v_cvt_scalef32_pk_fp8_f16 v150, v128, 1.0
	v_pk_fma_f16 v128, v128, v128, -2.0 op_sel:[0,1,1] op_sel_hi:[1,1,0]
	v_cvt_scalef32_pk_fp8_f16 v149, v130, 1.0 op_sel:[0,0,1]
	v_cvt_scalef32_pk_fp8_f16 v151, v203, 1.0 op_sel:[0,0,1]
	v_cvt_scalef32_pk_fp8_f16 v150, v128, 1.0 op_sel:[0,0,1]
	v_mfma_scale_f32_32x32x64_f8f6f4 v[48:63], v[170:177], v[152:159], v[48:63], v227, v226 op_sel_hi:[0,0,0]
	v_mfma_scale_f32_32x32x64_f8f6f4 v[16:31], v[162:169], v[152:159], v[16:31], v227, v226 op_sel_hi:[0,0,0]
	v_pk_fma_f16 v130, v160, v160, -2.0 op_sel:[0,1,1] op_sel_hi:[1,1,0]
	s_nop 0
	v_pk_fma_f16 v131, v130, v130, -2.0 op_sel:[0,1,1] op_sel_hi:[1,1,0]
	ds_read_b128 v[152:155], v234 offset:24576
	ds_read_b128 v[156:159], v234 offset:25600
	ds_read_b128 v[162:165], v234 offset:26624
	ds_read_b128 v[166:169], v234 offset:27648
	v_pk_fma_f16 v128, v131, v131, -2.0 op_sel:[0,1,1] op_sel_hi:[1,1,0]
	v_mov_b32_e32 v160, v204
	v_pk_fma_f16 v132, v128, v128, -2.0 op_sel:[0,1,1] op_sel_hi:[1,1,0]
	v_cvt_scalef32_pk_fp8_f16 v129, v128, 1.0
	v_cvt_scalef32_pk_fp8_f16 v129, v132, 1.0 op_sel:[0,0,1]
	v_mul_f32_e32 v132, 0.15915494, v179
	v_sin_f32_e32 v133, v132
	v_cos_f32_e32 v132, v132
	v_cvt_scalef32_pk_fp8_f16 v128, v130, 1.0
	v_cvt_scalef32_pk_fp8_f16 v128, v131, 1.0 op_sel:[0,0,1]
	v_add_f32_e32 v130, v132, v132
	v_cvt_pk_f16_f32 v132, v133, v130
	v_pk_fma_f16 v133, v132, v132, -2.0 op_sel:[1,0,1] op_sel_hi:[1,1,0]
	s_nop 0
	v_pk_fma_f16 v130, v133, v133, -2.0 op_sel:[0,1,1] op_sel_hi:[1,1,0]
	s_waitcnt lgkmcnt(2)
	v_mfma_scale_f32_32x32x64_f8f6f4 v[96:111], v[152:159], v[136:143], v[96:111], v227, v226 op_sel_hi:[0,0,0]
	v_cvt_scalef32_pk_fp8_f16 v131, v130, 1.0
	v_pk_fma_f16 v134, v130, v130, -2.0 op_sel:[0,1,1] op_sel_hi:[1,1,0]
	v_cvt_scalef32_pk_fp8_f16 v130, v132, 1.0
	v_cvt_scalef32_pk_fp8_f16 v131, v134, 1.0 op_sel:[0,0,1]
	v_cvt_scalef32_pk_fp8_f16 v130, v133, 1.0 op_sel:[0,0,1]
	v_pk_fma_f16 v133, v134, v134, -2.0 op_sel:[0,1,1] op_sel_hi:[1,1,0]
	v_mul_f32_e32 v134, 0.15915494, v181
	v_cos_f32_e32 v135, v134
	v_sin_f32_e32 v134, v134
	v_cvt_scalef32_pk_fp8_f16 v132, v133, 1.0
	v_pk_fma_f16 v133, v133, v133, -2.0 op_sel:[0,1,1] op_sel_hi:[1,1,0]
	ds_read_b128 v[170:173], v234 offset:28672
	ds_read_b128 v[174:177], v234 offset:29696
	ds_read_b128 v[236:239], v234 offset:30720
	ds_read_b128 v[240:243], v234 offset:31744
	v_cvt_scalef32_pk_fp8_f16 v132, v133, 1.0 op_sel:[0,0,1]
	v_add_f32_e32 v133, v135, v135
	v_mfma_scale_f32_32x32x64_f8f6f4 v[112:127], v[152:159], v[144:151], v[112:127], v227, v226 op_sel_hi:[0,0,0]
	v_cvt_pk_f16_f32 v152, v134, v133
	v_mul_f32_e32 v153, 0.15915494, v188
	v_lshl_add_u64 v[134:135], v[160:161], 2, s[4:5]
	v_mul_f32_e32 v154, 0.15915494, v189
	global_load_dwordx4 v[178:181], v[134:135], off offset:32
	global_load_dwordx4 v[186:189], v[134:135], off offset:3488
	v_pk_fma_f16 v134, v152, v152, -2.0 op_sel:[1,0,1] op_sel_hi:[1,1,0]
	v_cvt_scalef32_pk_fp8_f16 v133, v152, 1.0
	v_pk_fma_f16 v152, v134, v134, -2.0 op_sel:[0,1,1] op_sel_hi:[1,1,0]
	v_cvt_scalef32_pk_fp8_f16 v133, v134, 1.0 op_sel:[0,0,1]
	v_pk_fma_f16 v155, v152, v152, -2.0 op_sel:[0,1,1] op_sel_hi:[1,1,0]
	s_nop 0
	v_pk_fma_f16 v134, v155, v155, -2.0 op_sel:[0,1,1] op_sel_hi:[1,1,0]
	s_nop 0
	v_pk_fma_f16 v156, v134, v134, -2.0 op_sel:[0,1,1] op_sel_hi:[1,1,0]
	v_cvt_scalef32_pk_fp8_f16 v135, v134, 1.0
	v_cvt_scalef32_pk_fp8_f16 v134, v152, 1.0
	v_pk_fma_f16 v152, v203, v203, -2.0 op_sel:[0,1,1] op_sel_hi:[1,1,0]
	v_cvt_scalef32_pk_fp8_f16 v134, v155, 1.0 op_sel:[0,0,1]
	v_pk_fma_f16 v155, v152, v152, -2.0 op_sel:[0,1,1] op_sel_hi:[1,1,0]
	s_waitcnt lgkmcnt(4)
	v_mfma_scale_f32_32x32x64_f8f6f4 v[64:79], v[162:169], v[136:143], v[64:79], v227, v226 op_sel_hi:[0,0,0]
	v_cvt_scalef32_pk_fp8_f16 v135, v156, 1.0 op_sel:[0,0,1]
	v_pk_fma_f16 v156, v155, v155, -2.0 op_sel:[0,1,1] op_sel_hi:[1,1,0]
	s_nop 0
	v_pk_fma_f16 v157, v156, v156, -2.0 op_sel:[0,1,1] op_sel_hi:[1,1,0]
	v_mfma_scale_f32_32x32x64_f8f6f4 v[80:95], v[162:169], v[144:151], v[80:95], v227, v226 op_sel_hi:[0,0,0]
	v_cvt_scalef32_pk_fp8_f16 v165, v156, 1.0
	v_cos_f32_e32 v156, v153
	v_sin_f32_e32 v153, v153
	v_cvt_scalef32_pk_fp8_f16 v164, v152, 1.0
	v_add_f32_e32 v152, v156, v156
	v_cvt_pk_f16_f32 v152, v153, v152
	v_pk_fma_f16 v153, v152, v152, -2.0 op_sel:[1,0,1] op_sel_hi:[1,1,0]
	v_cvt_scalef32_pk_fp8_f16 v166, v152, 1.0
	v_cvt_scalef32_pk_fp8_f16 v164, v155, 1.0 op_sel:[0,0,1]
	v_pk_fma_f16 v155, v153, v153, -2.0 op_sel:[0,1,1] op_sel_hi:[1,1,0]
	v_cvt_scalef32_pk_fp8_f16 v166, v153, 1.0 op_sel:[0,0,1]
	s_waitcnt lgkmcnt(0)
	v_mfma_scale_f32_32x32x64_f8f6f4 v[0:15], v[236:243], v[136:143], v[0:15], v227, v226 op_sel_hi:[0,0,0]
	v_cos_f32_e32 v153, v154
	v_cvt_scalef32_pk_fp8_f16 v167, v155, 1.0
	v_pk_fma_f16 v155, v155, v155, -2.0 op_sel:[0,1,1] op_sel_hi:[1,1,0]
	v_sin_f32_e32 v154, v154
	v_pk_fma_f16 v152, v155, v155, -2.0 op_sel:[0,1,1] op_sel_hi:[1,1,0]
	s_nop 0
	v_cvt_scalef32_pk_fp8_f16 v168, v152, 1.0
	v_pk_fma_f16 v152, v152, v152, -2.0 op_sel:[0,1,1] op_sel_hi:[1,1,0]
	s_nop 0
	v_cvt_scalef32_pk_fp8_f16 v168, v152, 1.0 op_sel:[0,0,1]
	v_add_f32_e32 v152, v153, v153
	v_cvt_scalef32_pk_fp8_f16 v165, v157, 1.0 op_sel:[0,0,1]
	v_cvt_scalef32_pk_fp8_f16 v167, v155, 1.0 op_sel:[0,0,1]
	v_mfma_scale_f32_32x32x64_f8f6f4 v[32:47], v[170:177], v[136:143], v[32:47], v227, v226 op_sel_hi:[0,0,0]
	v_cvt_pk_f16_f32 v136, v154, v152
	v_cvt_scalef32_pk_fp8_f16 v169, v136, 1.0
	v_pk_fma_f16 v136, v136, v136, -2.0 op_sel:[1,0,1] op_sel_hi:[1,1,0]
	s_nop 0
	v_cvt_scalef32_pk_fp8_f16 v169, v136, 1.0 op_sel:[0,0,1]
	v_pk_fma_f16 v136, v136, v136, -2.0 op_sel:[0,1,1] op_sel_hi:[1,1,0]
	s_nop 0
	v_pk_fma_f16 v137, v136, v136, -2.0 op_sel:[0,1,1] op_sel_hi:[1,1,0]
	s_nop 0
	v_pk_fma_f16 v138, v137, v137, -2.0 op_sel:[0,1,1] op_sel_hi:[1,1,0]
	s_nop 0
	v_pk_fma_f16 v139, v138, v138, -2.0 op_sel:[0,1,1] op_sel_hi:[1,1,0]
	v_mfma_scale_f32_32x32x64_f8f6f4 v[48:63], v[170:177], v[144:151], v[48:63], v227, v226 op_sel_hi:[0,0,0]
	v_cvt_scalef32_pk_fp8_f16 v171, v138, 1.0
	v_cvt_scalef32_pk_fp8_f16 v170, v136, 1.0
	v_cvt_scalef32_pk_fp8_f16 v171, v139, 1.0 op_sel:[0,0,1]
	v_cvt_scalef32_pk_fp8_f16 v170, v137, 1.0 op_sel:[0,0,1]
	v_mfma_scale_f32_32x32x64_f8f6f4 v[16:31], v[236:243], v[144:151], v[16:31], v227, v226 op_sel_hi:[0,0,0]
	v_mul_f32_e32 v152, 0.15915494, v225
	ds_read_b128 v[136:139], v234 offset:32768
	ds_read_b128 v[140:143], v234 offset:33792
	v_cos_f32_e32 v153, v152
	v_sin_f32_e32 v152, v152
	v_mov_b32_e32 v205, v161
	s_waitcnt lgkmcnt(0)
	v_mfma_scale_f32_32x32x64_f8f6f4 v[96:111], v[136:143], v[128:135], v[96:111], v227, v226 op_sel_hi:[0,0,0]
	v_add_f32_e32 v153, v153, v153
	v_cvt_pk_f16_f32 v158, v152, v153
	v_mov_b32_e32 v203, v161
	v_cndmask_b32_e64 v162, 0, v222, s[0:1]
	v_mul_f32_e32 v163, 0.15915494, v223
	v_pk_fma_f16 v159, v158, v158, -2.0 op_sel:[1,0,1] op_sel_hi:[1,1,0]
	v_cndmask_b32_e64 v172, 0, v224, s[0:1]
	v_pk_fma_f16 v156, v159, v159, -2.0 op_sel:[0,1,1] op_sel_hi:[1,1,0]
	s_nop 0
	v_pk_fma_f16 v160, v156, v156, -2.0 op_sel:[0,1,1] op_sel_hi:[1,1,0]
	v_cvt_scalef32_pk_fp8_f16 v157, v156, 1.0
	v_cvt_scalef32_pk_fp8_f16 v156, v158, 1.0
	v_cvt_scalef32_pk_fp8_f16 v156, v159, 1.0 op_sel:[0,0,1]
	v_mfma_scale_f32_32x32x64_f8f6f4 v[112:127], v[136:143], v[164:171], v[112:127], v227, v226 op_sel_hi:[0,0,0]
	ds_read_b128 v[136:139], v234 offset:34816
	ds_read_b128 v[140:143], v234 offset:35840
	ds_read_b128 v[144:147], v234 offset:36864
	ds_read_b128 v[148:151], v234 offset:37888
	ds_read_b128 v[236:239], v234 offset:38912
	ds_read_b128 v[240:243], v234 offset:39936
	v_lshl_add_u64 v[152:153], v[204:205], 2, s[4:5]
	v_lshl_add_u64 v[154:155], v[202:203], 2, s[4:5]
	global_load_dword v225, v[152:153], off offset:48
	global_load_dword v222, v[154:155], off
	global_load_dword v224, v[154:155], off offset:3456
	global_load_dword v223, v[152:153], off offset:3504
	v_cvt_scalef32_pk_fp8_f16 v157, v160, 1.0 op_sel:[0,0,1]
	s_waitcnt lgkmcnt(4)
	v_mfma_scale_f32_32x32x64_f8f6f4 v[64:79], v[136:143], v[128:135], v[64:79], v227, v226 op_sel_hi:[0,0,0]
	v_mfma_scale_f32_32x32x64_f8f6f4 v[80:95], v[136:143], v[164:171], v[80:95], v227, v226 op_sel_hi:[0,0,0]
	v_mul_f32_e32 v136, v207, v208
	v_fma_f32 v137, v208, v208, -2.0
	v_cndmask_b32_e64 v138, v137, v136, s[0:1]
	v_mul_f32_e32 v136, v136, v137
	v_fma_f32 v137, v137, v137, -2.0
	v_cndmask_b32_e64 v139, v137, v136, s[0:1]
	v_cvt_pk_fp8_f32 v159, v138, v139
	v_mul_f32_e32 v136, v136, v137
	v_fma_f32 v137, v137, v137, -2.0
	v_cndmask_b32_e64 v136, v137, v136, s[0:1]
	v_cvt_pk_fp8_f32 v159, v136, v162 op_sel:[0,0,1]
	v_pk_fma_f16 v136, v160, v160, -2.0 op_sel:[0,1,1] op_sel_hi:[1,1,0]
	v_mov_b32_e32 v160, v161
	v_pk_fma_f16 v137, v136, v136, -2.0 op_sel:[0,1,1] op_sel_hi:[1,1,0]
	v_cvt_scalef32_pk_fp8_f16 v158, v136, 1.0
	v_cos_f32_e32 v136, v163
	v_cvt_scalef32_pk_fp8_f16 v158, v137, 1.0 op_sel:[0,0,1]
	v_sin_f32_e32 v137, v163
	s_waitcnt lgkmcnt(0)
	v_mfma_scale_f32_32x32x64_f8f6f4 v[0:15], v[236:243], v[128:135], v[0:15], v227, v226 op_sel_hi:[0,0,0]
	v_add_f32_e32 v136, v136, v136
	v_mov_b32_e32 v162, v161
	v_cvt_pk_f16_f32 v138, v137, v136
	v_pk_fma_f16 v139, v138, v138, -2.0 op_sel:[1,0,1] op_sel_hi:[1,1,0]
	s_nop 0
	v_pk_fma_f16 v136, v139, v139, -2.0 op_sel:[0,1,1] op_sel_hi:[1,1,0]
	v_mov_b32_e32 v163, v161
	v_pk_fma_f16 v140, v136, v136, -2.0 op_sel:[0,1,1] op_sel_hi:[1,1,0]
	v_cvt_scalef32_pk_fp8_f16 v137, v136, 1.0
	v_cvt_scalef32_pk_fp8_f16 v136, v138, 1.0
	v_cvt_scalef32_pk_fp8_f16 v136, v139, 1.0 op_sel:[0,0,1]
	v_mul_f32_e32 v138, v209, v210
	v_fma_f32 v139, v210, v210, -2.0
	v_cndmask_b32_e64 v141, v139, v138, s[0:1]
	v_mul_f32_e32 v138, v138, v139
	v_fma_f32 v142, v139, v139, -2.0
	v_cndmask_b32_e64 v143, v142, v138, s[0:1]
	v_cvt_pk_fp8_f32 v139, v141, v143
	v_mfma_scale_f32_32x32x64_f8f6f4 v[32:47], v[144:151], v[128:135], v[32:47], v227, v226 op_sel_hi:[0,0,0]
	v_mul_f32_e32 v128, v138, v142
	v_fma_f32 v129, v142, v142, -2.0
	v_cndmask_b32_e64 v128, v129, v128, s[0:1]
	v_cvt_pk_fp8_f32 v139, v128, v172 op_sel:[0,0,1]
	v_pk_fma_f16 v128, v140, v140, -2.0 op_sel:[0,1,1] op_sel_hi:[1,1,0]
	s_nop 0
	v_cvt_scalef32_pk_fp8_f16 v138, v128, 1.0
	v_pk_fma_f16 v128, v128, v128, -2.0 op_sel:[0,1,1] op_sel_hi:[1,1,0]
	v_cvt_scalef32_pk_fp8_f16 v137, v140, 1.0 op_sel:[0,0,1]
	v_cvt_scalef32_pk_fp8_f16 v138, v128, 1.0 op_sel:[0,0,1]
	v_mov_b32_e32 v140, v161
	v_mov_b32_e32 v141, v161
	v_mov_b32_e32 v142, v161
	v_mov_b32_e32 v143, v161
	v_mfma_scale_f32_32x32x64_f8f6f4 v[48:63], v[144:151], v[164:171], v[48:63], v227, v226 op_sel_hi:[0,0,0]
	v_mfma_scale_f32_32x32x64_f8f6f4 v[16:31], v[236:243], v[164:171], v[16:31], v227, v226 op_sel_hi:[0,0,0]
	ds_read_b128 v[128:131], v234 offset:40960
	ds_read_b128 v[132:135], v234 offset:41984
	s_waitcnt lgkmcnt(0)
	v_mfma_scale_f32_32x32x64_f8f6f4 v[96:111], v[128:135], v[156:163], v[96:111], v227, v226 op_sel_hi:[0,0,0]
	v_mfma_scale_f32_32x32x64_f8f6f4 v[112:127], v[128:135], v[136:143], v[112:127], v227, v226 op_sel_hi:[0,0,0]
	ds_read_b128 v[128:131], v234 offset:43008
	ds_read_b128 v[132:135], v234 offset:44032
	s_waitcnt lgkmcnt(0)
	v_mfma_scale_f32_32x32x64_f8f6f4 v[64:79], v[128:135], v[156:163], v[64:79], v227, v226 op_sel_hi:[0,0,0]
	v_mfma_scale_f32_32x32x64_f8f6f4 v[80:95], v[128:135], v[136:143], v[80:95], v227, v226 op_sel_hi:[0,0,0]
	ds_read_b128 v[128:131], v234 offset:45056
	ds_read_b128 v[132:135], v234 offset:46080
	s_waitcnt lgkmcnt(0)
	v_mfma_scale_f32_32x32x64_f8f6f4 v[32:47], v[128:135], v[156:163], v[32:47], v227, v226 op_sel_hi:[0,0,0]
	v_mfma_scale_f32_32x32x64_f8f6f4 v[48:63], v[128:135], v[136:143], v[48:63], v227, v226 op_sel_hi:[0,0,0]
	ds_read_b128 v[128:131], v234 offset:47104
	ds_read_b128 v[132:135], v234 offset:48128
	ds_read_b128 v[174:177], v234 offset:49152
	ds_read_b128 v[208:211], v234 offset:50176
	ds_read_b128 v[212:215], v234 offset:53248
	ds_read_b128 v[236:239], v234 offset:54272
	s_waitcnt lgkmcnt(4)
	v_mfma_scale_f32_32x32x64_f8f6f4 v[0:15], v[128:135], v[156:163], v[0:15], v227, v226 op_sel_hi:[0,0,0]
	v_mfma_scale_f32_32x32x64_f8f6f4 v[16:31], v[128:135], v[136:143], v[16:31], v227, v226 op_sel_hi:[0,0,0]
	v_cvt_pk_bf16_f32 v162, v96, v97 clamp
	v_cvt_pk_bf16_f32 v163, v98, v99 clamp
	v_cvt_pk_bf16_f32 v164, v100, v101 clamp
	v_cvt_pk_bf16_f32 v165, v102, v103 clamp
	v_cvt_pk_bf16_f32 v166, v112, v113 clamp
	v_cvt_pk_bf16_f32 v167, v114, v115 clamp
	v_cvt_pk_bf16_f32 v168, v116, v117 clamp
	v_cvt_pk_bf16_f32 v169, v118, v119 clamp
	v_cvt_pk_bf16_f32 v170, v104, v105 clamp
	v_cvt_pk_bf16_f32 v171, v106, v107 clamp
	v_cvt_pk_bf16_f32 v172, v108, v109 clamp
	v_add_u32_e32 v128, 0, v206
	v_cvt_pk_bf16_f32 v173, v110, v111 clamp
	v_add_u32_e32 v235, 0x18000, v128
	v_cvt_pk_bf16_f32 v202, v120, v121 clamp
	ds_read_b128 v[128:131], v235
	ds_read_b128 v[132:135], v235 offset:32
	ds_read_b128 v[136:139], v235 offset:64
	ds_read_b128 v[140:143], v235 offset:96
	v_cvt_pk_bf16_f32 v203, v122, v123 clamp
	ds_read_b128 v[96:99], v235 offset:128
	ds_read_b128 v[100:103], v235 offset:160
	ds_read_b128 v[104:107], v235 offset:192
	ds_read_b128 v[108:111], v235 offset:224
	v_cvt_pk_bf16_f32 v204, v124, v125 clamp
	v_cvt_pk_bf16_f32 v64, v64, v65
	s_waitcnt lgkmcnt(4)
	v_mfma_f32_32x32x16_bf16 v[144:159], v[174:177], v[166:169], v[128:143]
	v_cvt_pk_bf16_f32 v205, v126, v127 clamp
	ds_read_b128 v[240:243], v234 offset:57344
	ds_read_b128 v[244:247], v234 offset:58368
	ds_read_b128 v[248:251], v234 offset:61440
	ds_read_b128 v[252:255], v234 offset:62464
	v_cvt_pk_bf16_f32 v65, v74, v75 clamp
	v_cndmask_b32_e64 v230, v230, 0, s[14:15]
	v_mfma_f32_32x32x16_bf16 v[128:143], v[174:177], v[162:165], v[128:143]
	v_pk_max_i16 v174, v64, 0
	v_cvt_pk_bf16_f32 v175, v66, v67 clamp
	v_cvt_pk_bf16_f32 v176, v68, v69 clamp
	v_cvt_pk_bf16_f32 v177, v70, v71 clamp
	s_waitcnt lgkmcnt(4)
	v_mfma_f32_32x32x16_bf16 v[112:127], v[208:211], v[166:169], v[96:111]
	v_cvt_pk_bf16_f32 v80, v80, v81 clamp
	v_cvt_pk_bf16_f32 v81, v82, v83 clamp
	v_cvt_pk_bf16_f32 v82, v84, v85 clamp
	v_cvt_pk_bf16_f32 v83, v86, v87 clamp
	v_mfma_f32_32x32x16_bf16 v[96:111], v[208:211], v[162:165], v[96:111]
	v_cvt_pk_bf16_f32 v64, v72, v73 clamp
	v_cvt_pk_bf16_f32 v66, v76, v77 clamp
	v_cvt_pk_bf16_f32 v67, v78, v79 clamp
	v_cvt_pk_bf16_f32 v68, v88, v89 clamp
	v_cvt_pk_bf16_f32 v69, v90, v91 clamp
	v_cvt_pk_bf16_f32 v70, v92, v93 clamp
	v_cvt_pk_bf16_f32 v71, v94, v95 clamp
	v_add_u32_e32 v160, 0x14000, v234
	v_mfma_f32_32x32x16_bf16 v[128:143], v[212:215], v[170:173], v[128:143]
	v_mfma_f32_32x32x16_bf16 v[144:159], v[212:215], v[202:205], v[144:159]
	v_mfma_f32_32x32x16_bf16 v[96:111], v[236:239], v[170:173], v[96:111]
	v_mfma_f32_32x32x16_bf16 v[112:127], v[236:239], v[202:205], v[112:127]
	v_cvt_pk_bf16_f32 v76, v32, v33 clamp
	v_cvt_pk_bf16_f32 v77, v34, v35 clamp
	v_cvt_pk_bf16_f32 v78, v36, v37 clamp
	v_cvt_pk_bf16_f32 v79, v38, v39 clamp
	v_cvt_pk_bf16_f32 v88, v48, v49 clamp
	v_cvt_pk_bf16_f32 v89, v50, v51 clamp
	v_cvt_pk_bf16_f32 v90, v52, v53 clamp
	v_cvt_pk_bf16_f32 v91, v54, v55 clamp
	s_waitcnt lgkmcnt(3)
	v_mfma_f32_32x32x16_bf16 v[128:143], v[240:243], v[174:177], v[128:143]
	v_cvt_pk_bf16_f32 v72, v40, v41 clamp
	v_cvt_pk_bf16_f32 v73, v42, v43 clamp
	v_cvt_pk_bf16_f32 v74, v44, v45 clamp
	v_mfma_f32_32x32x16_bf16 v[144:159], v[240:243], v[80:83], v[144:159]
	ds_read_b128 v[92:95], v233 offset:16384
	ds_read_b128 v[208:211], v233 offset:17408
	ds_read_b128 v[236:239], v233 offset:20480
	ds_read_b128 v[240:243], v233 offset:21504
	v_cvt_pk_bf16_f32 v75, v46, v47 clamp
	v_cvt_pk_bf16_f32 v84, v56, v57 clamp
	v_cvt_pk_bf16_f32 v85, v58, v59 clamp
	s_waitcnt lgkmcnt(6)
	v_mfma_f32_32x32x16_bf16 v[96:111], v[244:247], v[174:177], v[96:111]
	v_cvt_pk_bf16_f32 v86, v60, v61 clamp
	v_cvt_pk_bf16_f32 v87, v62, v63 clamp
	v_mfma_f32_32x32x16_bf16 v[112:127], v[244:247], v[80:83], v[112:127]
	s_waitcnt lgkmcnt(5)
	v_mfma_f32_32x32x16_bf16 v[128:143], v[248:251], v[64:67], v[128:143]
	v_mfma_f32_32x32x16_bf16 v[144:159], v[248:251], v[68:71], v[144:159]
	s_waitcnt lgkmcnt(4)
	v_mfma_f32_32x32x16_bf16 v[96:111], v[252:255], v[64:67], v[96:111]
	v_mfma_f32_32x32x16_bf16 v[112:127], v[252:255], v[68:71], v[112:127]
	v_cvt_pk_bf16_f32 v206, v0, v1 clamp
	v_cvt_pk_bf16_f32 v207, v2, v3 clamp
	s_waitcnt lgkmcnt(2)
	v_mfma_f32_32x32x16_bf16 v[96:111], v[208:211], v[76:79], v[96:111]
	ds_read_b128 v[32:35], v233 offset:24576
	ds_read_b128 v[36:39], v233 offset:25600
	ds_read_b128 v[40:43], v233 offset:28672
	ds_read_b128 v[44:47], v233 offset:29696
	v_mfma_f32_32x32x16_bf16 v[112:127], v[208:211], v[88:91], v[112:127]
	v_cvt_pk_bf16_f32 v208, v4, v5 clamp
	v_cvt_pk_bf16_f32 v209, v6, v7 clamp
	v_cvt_pk_bf16_f32 v214, v16, v17 clamp
	v_cvt_pk_bf16_f32 v215, v18, v19 clamp
	v_cvt_pk_bf16_f32 v216, v20, v21 clamp
	v_cvt_pk_bf16_f32 v217, v22, v23 clamp
	v_mfma_f32_32x32x16_bf16 v[128:143], v[92:95], v[76:79], v[128:143]
	v_mfma_f32_32x32x16_bf16 v[144:159], v[92:95], v[88:91], v[144:159]
	v_cvt_pk_bf16_f32 v92, v8, v9 clamp
	v_cvt_pk_bf16_f32 v93, v10, v11 clamp
	v_cvt_pk_bf16_f32 v94, v12, v13 clamp
	v_cvt_pk_bf16_f32 v95, v14, v15 clamp
	v_cvt_pk_bf16_f32 v210, v24, v25 clamp
	v_cvt_pk_bf16_f32 v211, v26, v27 clamp
	v_cvt_pk_bf16_f32 v212, v28, v29 clamp
	v_cvt_pk_bf16_f32 v213, v30, v31 clamp
	s_waitcnt lgkmcnt(5)
	v_mfma_f32_32x32x16_bf16 v[128:143], v[236:239], v[72:75], v[128:143]
	v_mfma_f32_32x32x16_bf16 v[144:159], v[236:239], v[84:87], v[144:159]
	s_waitcnt lgkmcnt(4)
	v_mfma_f32_32x32x16_bf16 v[96:111], v[240:243], v[72:75], v[96:111]
	v_mfma_f32_32x32x16_bf16 v[112:127], v[240:243], v[84:87], v[112:127]
	s_waitcnt lgkmcnt(3)
	v_mfma_f32_32x32x16_bf16 v[128:143], v[32:35], v[206:209], v[128:143]
	ds_read_b128 v[0:3], v234 offset:51200
	ds_read_b128 v[236:239], v234 offset:52224
	ds_read_b128 v[240:243], v234 offset:55296
	ds_read_b128 v[244:247], v234 offset:56320
	v_mfma_f32_32x32x16_bf16 v[144:159], v[32:35], v[214:217], v[144:159]
	s_waitcnt lgkmcnt(6)
	v_mfma_f32_32x32x16_bf16 v[96:111], v[36:39], v[206:209], v[96:111]
	v_mfma_f32_32x32x16_bf16 v[112:127], v[36:39], v[214:217], v[112:127]
	s_waitcnt lgkmcnt(5)
	v_mfma_f32_32x32x16_bf16 v[128:143], v[40:43], v[92:95], v[128:143]
	v_mfma_f32_32x32x16_bf16 v[144:159], v[40:43], v[210:213], v[144:159]
	s_waitcnt lgkmcnt(4)
	v_mfma_f32_32x32x16_bf16 v[96:111], v[44:47], v[92:95], v[96:111]
	v_mfma_f32_32x32x16_bf16 v[112:127], v[44:47], v[210:213], v[112:127]
	ds_read_b128 v[32:35], v235 offset:256
	ds_read_b128 v[36:39], v235 offset:288
	ds_read_b128 v[40:43], v235 offset:320
	ds_read_b128 v[44:47], v235 offset:352
	s_nop 3
	v_cvt_pk_bf16_f32 v128, v128, v129 clamp
	v_cvt_pk_bf16_f32 v129, v130, v131 clamp
	v_cvt_pk_bf16_f32 v130, v132, v133 clamp
	v_cvt_pk_bf16_f32 v131, v134, v135 clamp
	s_waitcnt lgkmcnt(0)
	v_mfma_f32_32x32x16_bf16 v[48:63], v[0:3], v[166:169], v[32:47]
	v_cvt_pk_bf16_f32 v132, v144, v145 clamp
	v_cvt_pk_bf16_f32 v133, v146, v147 clamp
	v_cvt_pk_bf16_f32 v134, v148, v149 clamp
	v_cvt_pk_bf16_f32 v135, v150, v151 clamp
	v_mfma_f32_32x32x16_bf16 v[32:47], v[0:3], v[162:165], v[32:47]
	ds_read_b128 v[0:3], v235 offset:384
	ds_read_b128 v[4:7], v235 offset:416
	ds_read_b128 v[8:11], v235 offset:448
	ds_read_b128 v[12:15], v235 offset:480
	s_waitcnt lgkmcnt(0)
	v_mfma_f32_32x32x16_bf16 v[16:31], v[236:239], v[166:169], v[0:15]
	v_mfma_f32_32x32x16_bf16 v[0:15], v[236:239], v[162:165], v[0:15]
	ds_read_b128 v[162:165], v234 offset:59392
	ds_read_b128 v[166:169], v234 offset:60416
	ds_read_b128 v[236:239], v234 offset:63488
	ds_read_b128 v[248:251], v234 offset:64512
	v_mfma_f32_32x32x16_bf16 v[0:15], v[244:247], v[170:173], v[0:15]
	v_mfma_f32_32x32x16_bf16 v[32:47], v[240:243], v[170:173], v[32:47]
	v_mfma_f32_32x32x16_bf16 v[48:63], v[240:243], v[202:205], v[48:63]
	v_mfma_f32_32x32x16_bf16 v[16:31], v[244:247], v[202:205], v[16:31]
	s_waitcnt lgkmcnt(2)
	v_mfma_f32_32x32x16_bf16 v[0:15], v[166:169], v[174:177], v[0:15]
	v_cvt_pk_bf16_f32 v136, v136, v137 clamp
	v_cvt_pk_bf16_f32 v137, v138, v139 clamp
	v_cvt_pk_bf16_f32 v138, v140, v141 clamp
	v_cvt_pk_bf16_f32 v139, v142, v143 clamp
	v_cvt_pk_bf16_f32 v140, v152, v153 clamp
	v_mfma_f32_32x32x16_bf16 v[32:47], v[162:165], v[174:177], v[32:47]
	v_mfma_f32_32x32x16_bf16 v[48:63], v[162:165], v[80:83], v[48:63]
	v_mfma_f32_32x32x16_bf16 v[16:31], v[166:169], v[80:83], v[16:31]
	ds_read_b128 v[80:83], v233 offset:18432
	ds_read_b128 v[144:147], v233 offset:19456
	ds_read_b128 v[148:151], v233 offset:22528
	ds_read_b128 v[162:165], v233 offset:23552
	s_waitcnt lgkmcnt(4)
	v_mfma_f32_32x32x16_bf16 v[0:15], v[248:251], v[64:67], v[0:15]
	v_mfma_f32_32x32x16_bf16 v[32:47], v[236:239], v[64:67], v[32:47]
	v_cvt_pk_bf16_f32 v141, v154, v155 clamp
	v_cvt_pk_bf16_f32 v142, v156, v157 clamp
	v_cvt_pk_bf16_f32 v143, v158, v159 clamp
	v_mfma_f32_32x32x16_bf16 v[48:63], v[236:239], v[68:71], v[48:63]
	v_mfma_f32_32x32x16_bf16 v[16:31], v[248:251], v[68:71], v[16:31]
	s_waitcnt lgkmcnt(2)
	v_mfma_f32_32x32x16_bf16 v[0:15], v[144:147], v[76:79], v[0:15]
	v_mfma_f32_32x32x16_bf16 v[32:47], v[80:83], v[76:79], v[32:47]
	v_mfma_f32_32x32x16_bf16 v[48:63], v[80:83], v[88:91], v[48:63]
	ds_read_b128 v[64:67], v233 offset:26624
	ds_read_b128 v[68:71], v233 offset:27648
	ds_read_b128 v[76:79], v233 offset:30720
	ds_read_b128 v[80:83], v233 offset:31744
	v_mfma_f32_32x32x16_bf16 v[16:31], v[144:147], v[88:91], v[16:31]
	v_cvt_pk_bf16_f32 v96, v96, v97 clamp
	v_cvt_pk_bf16_f32 v97, v98, v99 clamp
	v_cvt_pk_bf16_f32 v98, v100, v101 clamp
	v_cvt_pk_bf16_f32 v99, v102, v103 clamp
	s_waitcnt lgkmcnt(4)
	v_mfma_f32_32x32x16_bf16 v[0:15], v[162:165], v[72:75], v[0:15]
	v_cvt_pk_bf16_f32 v100, v112, v113 clamp
	v_mfma_f32_32x32x16_bf16 v[32:47], v[148:151], v[72:75], v[32:47]
	v_cvt_pk_bf16_f32 v101, v114, v115 clamp
	v_cvt_pk_bf16_f32 v102, v116, v117 clamp
	v_cvt_pk_bf16_f32 v103, v118, v119 clamp
	v_mfma_f32_32x32x16_bf16 v[48:63], v[148:151], v[84:87], v[48:63]
	v_mfma_f32_32x32x16_bf16 v[16:31], v[162:165], v[84:87], v[16:31]
	s_waitcnt lgkmcnt(2)
	v_mfma_f32_32x32x16_bf16 v[0:15], v[68:71], v[206:209], v[0:15]
	ds_read_b128 v[84:87], v160
	ds_read_b128 v[112:115], v160 offset:1024
	ds_read_b128 v[116:119], v160 offset:2048
	ds_read_b128 v[144:147], v160 offset:3072
	v_mfma_f32_32x32x16_bf16 v[32:47], v[64:67], v[206:209], v[32:47]
	v_mfma_f32_32x32x16_bf16 v[48:63], v[64:67], v[214:217], v[48:63]
	v_cvt_pk_bf16_f32 v104, v104, v105 clamp
	v_cvt_pk_bf16_f32 v105, v106, v107 clamp
	v_cvt_pk_bf16_f32 v106, v108, v109 clamp
	v_cvt_pk_bf16_f32 v107, v110, v111 clamp
	v_mfma_f32_32x32x16_bf16 v[16:31], v[68:71], v[214:217], v[16:31]
	v_cvt_pk_bf16_f32 v108, v120, v121 clamp
	v_cvt_pk_bf16_f32 v109, v122, v123 clamp
	v_cvt_pk_bf16_f32 v110, v124, v125 clamp
	s_waitcnt lgkmcnt(4)
	v_mfma_f32_32x32x16_bf16 v[0:15], v[80:83], v[92:95], v[0:15]
	v_cvt_pk_bf16_f32 v111, v126, v127 clamp
	v_mfma_f32_32x32x16_bf16 v[32:47], v[76:79], v[92:95], v[32:47]
	v_mfma_f32_32x32x16_bf16 v[48:63], v[76:79], v[210:213], v[48:63]
	v_mfma_f32_32x32x16_bf16 v[16:31], v[80:83], v[210:213], v[16:31]
	s_waitcnt lgkmcnt(3)
	v_mfma_f32_4x4x4_16b_bf16 v[64:67], v[84:85], v[128:129], 0
	v_mfma_f32_4x4x4_16b_bf16 v[68:71], v[86:87], v[130:131], 0
	s_nop 7
	v_cvt_pk_bf16_f32 v32, v32, v33 clamp
	v_cvt_pk_bf16_f32 v33, v34, v35 clamp
	v_cvt_pk_bf16_f32 v34, v36, v37 clamp
	v_cvt_pk_bf16_f32 v35, v38, v39 clamp
	v_mfma_f32_4x4x4_16b_bf16 v[80:83], v[84:85], v[132:133], 0
	v_mfma_f32_4x4x4_16b_bf16 v[88:91], v[86:87], v[134:135], 0
	v_cvt_pk_bf16_f32 v48, v48, v49 clamp
	v_cvt_pk_bf16_f32 v49, v50, v51 clamp
	v_cvt_pk_bf16_f32 v50, v52, v53 clamp
	v_cvt_pk_bf16_f32 v51, v54, v55 clamp
	s_waitcnt lgkmcnt(2)
	v_mfma_f32_4x4x4_16b_bf16 v[64:67], v[112:113], v[136:137], v[64:67]
	v_mfma_f32_4x4x4_16b_bf16 v[68:71], v[114:115], v[138:139], v[68:71]
	v_cvt_pk_bf16_f32 v40, v40, v41 clamp
	v_cvt_pk_bf16_f32 v41, v42, v43 clamp
	v_cvt_pk_bf16_f32 v42, v44, v45 clamp
	v_cvt_pk_bf16_f32 v43, v46, v47 clamp
	v_mfma_f32_4x4x4_16b_bf16 v[80:83], v[112:113], v[140:141], v[80:83]
	v_mfma_f32_4x4x4_16b_bf16 v[88:91], v[114:115], v[142:143], v[88:91]
	s_waitcnt lgkmcnt(1)
	v_mfma_f32_4x4x4_16b_bf16 v[64:67], v[116:117], v[96:97], v[64:67]
	v_mfma_f32_4x4x4_16b_bf16 v[68:71], v[118:119], v[98:99], v[68:71]
	ds_read_b128 v[36:39], v160 offset:4096
	ds_read_b128 v[96:99], v160 offset:5120
	v_cvt_pk_bf16_f32 v0, v0, v1 clamp
	v_cvt_pk_bf16_f32 v1, v2, v3 clamp
	v_cvt_pk_bf16_f32 v2, v4, v5 clamp
	v_cvt_pk_bf16_f32 v3, v6, v7 clamp
	v_mfma_f32_4x4x4_16b_bf16 v[80:83], v[116:117], v[100:101], v[80:83]
	v_mfma_f32_4x4x4_16b_bf16 v[88:91], v[118:119], v[102:103], v[88:91]
	ds_read_b128 v[4:7], v160 offset:7168
	v_cvt_pk_bf16_f32 v12, v12, v13
	v_cvt_pk_bf16_f32 v24, v24, v25
	v_cvt_pk_bf16_f32 v25, v26, v27
	s_waitcnt lgkmcnt(3)
	v_mfma_f32_4x4x4_16b_bf16 v[64:67], v[144:145], v[104:105], v[64:67]
	v_mfma_f32_4x4x4_16b_bf16 v[68:71], v[146:147], v[106:107], v[68:71]
	v_cndmask_b32_e64 v219, v219, 0, s[14:15]
	v_cndmask_b32_e64 v218, v218, 0, s[14:15]
	v_mfma_f32_4x4x4_16b_bf16 v[80:83], v[144:145], v[108:109], v[80:83]
	v_mfma_f32_4x4x4_16b_bf16 v[88:91], v[146:147], v[110:111], v[88:91]
	s_waitcnt lgkmcnt(2)
	v_mfma_f32_4x4x4_16b_bf16 v[64:67], v[36:37], v[32:33], v[64:67]
	v_mfma_f32_4x4x4_16b_bf16 v[68:71], v[38:39], v[34:35], v[68:71]
	v_cvt_pk_bf16_f32 v34, v20, v21
	v_cvt_pk_bf16_f32 v35, v22, v23
	ds_read_b128 v[20:23], v160 offset:6144
	v_cvt_pk_bf16_f32 v32, v16, v17
	v_cvt_pk_bf16_f32 v33, v18, v19
	v_cvt_pk_bf16_f32 v16, v56, v57 clamp
	v_cvt_pk_bf16_f32 v17, v58, v59 clamp
	v_mfma_f32_4x4x4_16b_bf16 v[80:83], v[36:37], v[48:49], v[80:83]
	v_mfma_f32_4x4x4_16b_bf16 v[88:91], v[38:39], v[50:51], v[88:91]
	v_cvt_pk_bf16_f32 v18, v60, v61 clamp
	v_cvt_pk_bf16_f32 v19, v62, v63 clamp
	s_waitcnt lgkmcnt(2)
	v_mfma_f32_4x4x4_16b_bf16 v[64:67], v[96:97], v[40:41], v[64:67]
	v_mfma_f32_4x4x4_16b_bf16 v[68:71], v[98:99], v[42:43], v[68:71]
	v_mfma_f32_4x4x4_16b_bf16 v[80:83], v[96:97], v[16:17], v[80:83]
	v_mfma_f32_4x4x4_16b_bf16 v[88:91], v[98:99], v[18:19], v[88:91]
	v_cvt_pk_bf16_f32 v16, v8, v9
	v_cvt_pk_bf16_f32 v17, v10, v11
	v_pk_max_i16 v8, v24, 0
	v_pk_max_i16 v9, v25, 0
	v_cvt_pk_bf16_f32 v10, v28, v29 clamp
	v_cvt_pk_bf16_f32 v11, v30, v31 clamp
	s_waitcnt lgkmcnt(0)
	v_mfma_f32_4x4x4_16b_bf16 v[64:67], v[20:21], v[0:1], v[64:67]
	v_mfma_f32_4x4x4_16b_bf16 v[68:71], v[22:23], v[2:3], v[68:71]
	v_pk_max_i16 v0, v32, 0
	v_pk_max_i16 v1, v33, 0
	v_pk_max_i16 v2, v34, 0
	v_pk_max_i16 v3, v35, 0
	s_nop 1
	v_mfma_f32_4x4x4_16b_bf16 v[80:83], v[20:21], v[0:1], v[80:83]
	v_mfma_f32_4x4x4_16b_bf16 v[88:91], v[22:23], v[2:3], v[88:91]
	v_pk_max_i16 v0, v16, 0
	v_pk_max_i16 v1, v17, 0
	v_pk_max_i16 v2, v12, 0
	v_cvt_pk_bf16_f32 v3, v14, v15 clamp
	s_nop 1
	v_mfma_f32_4x4x4_16b_bf16 v[64:67], v[4:5], v[0:1], v[64:67]
	v_mfma_f32_4x4x4_16b_bf16 v[68:71], v[6:7], v[2:3], v[68:71]
	v_mfma_f32_4x4x4_16b_bf16 v[80:83], v[4:5], v[8:9], v[80:83]
	v_mfma_f32_4x4x4_16b_bf16 v[88:91], v[6:7], v[10:11], v[88:91]
	s_waitcnt vmcnt(10)
	s_nop 3
	v_pk_add_f32 v[64:65], v[64:65], v[68:69]
	v_pk_add_f32 v[80:81], v[80:81], v[88:89]
	v_add_f32_e32 v66, v66, v70
	v_add_f32_e32 v82, v82, v90
	s_nop 1
	v_permlane32_swap_b32_e32 v64, v80
	v_permlane32_swap_b32_e32 v65, v81
	v_permlane32_swap_b32_e32 v66, v82
	s_nop 0
	v_add_f32_e32 v64, v64, v80
	v_add_f32_e32 v65, v65, v81
	v_add_f32_e32 v66, v66, v82
	v_add_f32_e32 v3, s10, v64
	v_add_f32_e32 v4, s11, v65
	v_add_f32_e32 v5, s18, v66
	v_mul_f32_e32 v3, 0xbfb8aa3b, v3
	v_mul_f32_e32 v4, 0xbfb8aa3b, v4
	v_mul_f32_e32 v5, 0xbfb8aa3b, v5
	v_exp_f32_e32 v3, v3
	v_exp_f32_e32 v4, v4
	v_exp_f32_e32 v5, v5
	v_add_f32_e32 v3, 1.0, v3
	v_add_f32_e32 v4, 1.0, v4
	v_add_f32_e32 v5, 1.0, v5
	v_rcp_f32_e32 v3, v3
	v_rcp_f32_e32 v4, v4
	v_rcp_f32_e32 v5, v5
	v_fmac_f32_e32 v218, v232, v3
	v_fmac_f32_e32 v219, v232, v4
	v_fmac_f32_e32 v230, v232, v5
	s_andn2_b64 vcc, exec, s[12:13]
	s_cbranch_vccnz .LBB1_6
	v_add_f32_dpp v218, v218, v218 row_shr:1 row_mask:0xf bank_mask:0xf bound_ctrl:1
	v_add_f32_dpp v219, v219, v219 row_shr:1 row_mask:0xf bank_mask:0xf bound_ctrl:1
	v_add_f32_dpp v230, v230, v230 row_shr:1 row_mask:0xf bank_mask:0xf bound_ctrl:1
	v_add_f32_dpp v218, v218, v218 row_shr:2 row_mask:0xf bank_mask:0xf bound_ctrl:1
	v_add_f32_dpp v219, v219, v219 row_shr:2 row_mask:0xf bank_mask:0xf bound_ctrl:1
	v_add_f32_dpp v230, v230, v230 row_shr:2 row_mask:0xf bank_mask:0xf bound_ctrl:1
	v_add_f32_dpp v218, v218, v218 row_shr:4 row_mask:0xf bank_mask:0xf bound_ctrl:1
	v_add_f32_dpp v219, v219, v219 row_shr:4 row_mask:0xf bank_mask:0xf bound_ctrl:1
	v_add_f32_dpp v230, v230, v230 row_shr:4 row_mask:0xf bank_mask:0xf bound_ctrl:1
	v_add_f32_dpp v218, v218, v218 row_shr:8 row_mask:0xf bank_mask:0xf bound_ctrl:1
	v_add_f32_dpp v219, v219, v219 row_shr:8 row_mask:0xf bank_mask:0xf bound_ctrl:1
	v_add_f32_dpp v230, v230, v230 row_shr:8 row_mask:0xf bank_mask:0xf bound_ctrl:1
	v_mov_b32_e32 v0, 0
	v_mov_b32_e32 v1, 0
	v_mov_b32_e32 v5, 0
	v_mov_b32_dpp v0, v218 row_bcast:15 row_mask:0xa bank_mask:0xf
	v_mov_b32_dpp v1, v219 row_bcast:15 row_mask:0xa bank_mask:0xf
	v_mov_b32_dpp v5, v230 row_bcast:15 row_mask:0xa bank_mask:0xf
	v_lshl_add_u32 v6, v231, 1, v231
	v_ashrrev_i32_e32 v7, 31, v6
	v_add_f32_e32 v218, v218, v0
	v_add_f32_e32 v219, v219, v1
	v_add_f32_e32 v230, v230, v5
	v_mov_b32_e32 v0, 0
	v_mov_b32_e32 v1, 0
	v_mov_b32_e32 v5, 0
	v_mov_b32_dpp v0, v218 row_bcast:31 row_mask:0xc bank_mask:0xf
	v_mov_b32_dpp v1, v219 row_bcast:31 row_mask:0xc bank_mask:0xf
	v_mov_b32_dpp v5, v230 row_bcast:31 row_mask:0xc bank_mask:0xf
	v_lshl_add_u64 v[6:7], v[6:7], 2, s[8:9]
	v_cmp_eq_u32_e32 vcc, 63, v220
	v_add_f32_e32 v2, v218, v0
	v_add_f32_e32 v3, v219, v1
	v_add_f32_e32 v4, v230, v5
	s_and_saveexec_b64 s[12:13], vcc
	global_store_dwordx3 v[6:7], v[2:4], off
	s_branch .LBB1_5
